# attn: hand-generated fast path - VT tile staged once in LDS during EA wait, software-pipelined MFMA/VALU loop with A operands staged in unused accumulator rows, Wo load inside loop
# baseline (speedup 1.0000x reference)
_Z11attn_kernelPKfS0_PKDF16_S0_S0_S0_S2_PDF16_S3_:
	s_load_dwordx16 s[4:19], s[0:1], 0x0
	s_load_dwordx2 s[62:63], s[0:1], 0x40
	v_readfirstlane_b32 s49, v0
	s_and_b32 s22, s2, 7
	s_lshr_b32 s23, s2, 3
	s_lshl_b32 s43, s22, 1
	s_and_b32 s24, s23, 1
	s_or_b32 s33, s43, s24
	s_lshr_b32 s41, s2, 4
	s_mul_i32 s41, s41, 24
	s_lshr_b32 s51, s49, 6
	s_mul_i32 s34, s33, 0xc0
	s_mov_b32 s35, 0
	s_lshl_b32 s25, s33, 5
	s_lshl_b32 s42, s22, 5
	s_add_i32 s42, s42, s23
	s_lshl_b32 s42, s42, 10
	s_add_i32 s36, s41, 23
	s_lshr_b32 s36, s36, 4
	s_and_b32 s36, s36, 0xffffffc
	s_lshr_b32 s37, s41, 4
	s_and_b32 s37, s37, 0xffffffc
	s_movk_i32 s40, 0x200
	v_lshrrev_b32_e32 v34, 5, v0
	v_bfe_u32 v35, v0, 1, 4
	v_mov_b32_e32 v115, 0
	v_lshlrev_b32_e32 v116, 4, v0
	v_add_u32_e32 v2, s41, v34
	v_lshrrev_b32_e32 v2, 1, v2
	v_mov_b32_e32 v3, v115
	v_lshl_add_u64 v[2:3], s[34:35], 0, v[2:3]
	v_lshlrev_b64 v[2:3], 9, v[2:3]
	v_lshlrev_b32_e32 v4, 5, v35
	v_mov_b32_e32 v5, v115
	v_lshrrev_b32_e32 v8, 3, v0
	v_and_b32_e32 v8, 4, v8
	v_mov_b32_e32 v9, v115
	v_lshrrev_b32_e32 v36, 2, v0
	s_movk_i32 s26, 0xab
	v_mul_u32_u24_e32 v36, s26, v36
	v_lshrrev_b32_e32 v36, 9, v36
	v_mul_u32_u24_e32 v37, 12, v36
	v_sub_u32_e32 v37, v0, v37
	s_lshl_b32 s27, s33, 6
	v_add_u32_e32 v38, s27, v36
	v_mul_u32_u24_e32 v38, 0x300, v38
	v_lshl_add_u32 v38, v37, 6, v38
	v_mul_u32_u24_e32 v39, 0x320, v36
	v_lshl_add_u32 v39, v37, 6, v39
	s_waitcnt lgkmcnt(0)
	s_add_u32 s26, s12, s25
	s_addc_u32 s27, s13, 0
	s_load_dword s52, s[26:27], s36 offset:0x0
	s_load_dword s53, s[26:27], s37 offset:0x0
	s_load_dwordx4 s[56:59], s[12:13], s25 offset:0x200
	s_load_dwordx2 s[60:61], s[12:13], s25 offset:0x210
	s_load_dwordx2 s[28:29], s[12:13], 0x400
	v_lshl_add_u64 v[2:3], s[4:5], 0, v[2:3]
	v_lshl_add_u64 v[6:7], v[2:3], 0, v[4:5]
	v_lshlrev_b32_e32 v2, 4, v35
	v_lshl_add_u64 v[10:11], v[6:7], 0, v[8:9]
	global_load_dwordx4 v[2:5], v2, s[10:11]
	s_nop 0
	global_load_dword v8, v[10:11], off offset:24
	global_load_dword v6, v[10:11], off
	global_load_dword v7, v[10:11], off offset:8
	global_load_dword v9, v[10:11], off offset:16
	global_load_dwordx4 v[66:69], v38, s[8:9]
	global_load_dwordx4 v[70:73], v38, s[8:9] offset:16
	global_load_dwordx4 v[74:77], v38, s[8:9] offset:32
	global_load_dwordx4 v[78:81], v38, s[8:9] offset:48
	s_waitcnt lgkmcnt(0)
	v_max_f32_e64 v10, s52, s52
	v_max_f32_e64 v11, s53, s53
	v_max_f32_e32 v10, v11, v10
	v_max_f32_e64 v11, s57, s57
	v_max_f32_e64 v12, s56, s56
	v_max_f32_e32 v11, v12, v11
	v_max_f32_e64 v12, s59, s59
	v_max_f32_e64 v13, s58, s58
	v_max_f32_e32 v12, v13, v12
	v_max_f32_e64 v13, s61, s61
	v_max_f32_e64 v14, s60, s60
	v_max_f32_e32 v13, v14, v13
	v_max3_f32 v11, v11, v12, v13
	s_mov_b32 s24, 0x41700000
	v_cmp_gt_f32_e32 vcc, s24, v10
	v_cmp_gt_f32_e64 s[26:27], s24, v11
	s_and_b64 s[26:27], vcc, s[26:27]
	v_cmp_lt_f32_e64 s[36:37], s29, 4.0
	s_and_b64 s[26:27], s[26:27], s[36:37]
	v_max_f32_e32 v12, v10, v10
	v_max_f32_e32 v12, 1.0, v12
	v_mul_f32_e32 v13, v12, v12
	v_mul_f32_e32 v13, v12, v13
	v_mul_f32_e32 v12, v12, v13
	v_mul_f32_e32 v12, s29, v12
	s_mov_b32 s24, 0x476a6000
	v_cmp_gt_f32_e64 s[36:37], s24, v12
	s_and_b64 s[26:27], s[26:27], s[36:37]
	s_andn2_b64 vcc, exec, s[26:27]
	s_cbranch_vccz .Lf_fast
	s_waitcnt vmcnt(0)
	s_branch .Lattn_orig
.Lf_fast:
	v_and_b32_e32 v15, 1, v0
	v_cmp_eq_u32_e32 vcc, 0, v15
	s_waitcnt vmcnt(8)
	v_mov_b32_e32 v10, v2
	v_mov_b32_e32 v11, v4
	v_mov_b32_e32 v12, v3
	v_cndmask_b32_e32 v13, 0, v5, vcc
	s_waitcnt vmcnt(7)
	v_cndmask_b32_e64 v14, v8, 1.0, vcc
	v_pk_add_f32 v[10:11], v[10:11], v[12:13]
	s_waitcnt vmcnt(5)
	v_pk_mul_f32 v[12:13], v[6:7], v[14:15] op_sel_hi:[1,0]
	v_pk_add_f32 v[10:11], v[10:11], v[10:11] op_sel:[0,1] op_sel_hi:[1,0]
	v_mov_b32_e32 v8, v6
	v_mov_b32_e32 v16, v13
	v_pk_add_f32 v[22:23], v[10:11], v[2:3] op_sel_hi:[0,1] neg_lo:[0,1] neg_hi:[0,1]
	v_mov_b32_e32 v17, v14
	s_waitcnt vmcnt(4)
	v_pk_mul_f32 v[8:9], v[8:9], v[16:17]
	v_mov_b32_e32 v16, v22
	v_mov_b32_e32 v17, v10
	v_mov_b32_e32 v2, v3
	v_mov_b32_e32 v3, v4
	v_fma_mixlo_f16 v5, v14, v10, 0
	v_pk_add_f32 v[10:11], v[16:17], v[2:3] neg_lo:[0,1] neg_hi:[0,1]
	v_pk_mul_f32 v[2:3], v[12:13], v[22:23]
	v_pk_add_f32 v[16:17], v[22:23], v[4:5] op_sel_hi:[1,0] neg_lo:[0,1] neg_hi:[0,1]
	v_cvt_pk_f16_f32 v3, v2, v3
	v_sub_f32_e32 v22, v10, v4
	v_pack_b32_f16 v2, v5, v3
	v_pk_mul_f32 v[4:5], v[8:9], v[10:11]
	v_pk_mul_f32 v[10:11], v[6:7], v[8:9] op_sel:[0,1]
	v_cvt_pk_f16_f32 v23, v4, v5
	v_pk_mul_f32 v[4:5], v[10:11], v[16:17]
	v_lshlrev_b32_e32 v7, 7, v35
	v_cvt_pk_f16_f32 v5, v4, v5
	v_lshlrev_b32_e32 v15, 5, v15
	v_mul_f32_e32 v6, v6, v11
	v_alignbit_b32 v4, v5, v23, 16
	v_lshrrev_b32_e32 v5, 16, v5
	v_or3_b32 v7, v7, v15, v34
	v_alignbit_b32 v3, v23, v3, 16
	v_fma_mixhi_f16 v5, v6, v22, 0
	v_lshl_add_u32 v7, v7, 4, 0
	ds_write_b128 v7, v[2:5]
	v_cvt_pk_f16_f32 v2, v14, v12
	v_cvt_pk_f16_f32 v3, v13, v8
	v_cvt_pk_f16_f32 v4, v9, v10
	v_cvt_pk_f16_f32 v5, v11, v6
	v_cmp_gt_u32_e32 vcc, s40, v0
	ds_write_b128 v7, v[2:5] offset:1024
	s_and_saveexec_b64 s[2:3], vcc
	s_cbranch_execz .Lf_27
	v_lshlrev_b32_e32 v2, 2, v0
	v_and_b32_e32 v3, 7, v0
	s_movk_i32 s4, 0x7e0
	v_and_or_b32 v2, v2, s4, v3
	v_lshl_add_u32 v2, v2, 4, 0
	v_mov_b32_e32 v4, v115
	v_mov_b32_e32 v5, v115
	v_mov_b32_e32 v6, v115
	v_mov_b32_e32 v7, v115
	ds_write_b128 v2, v[4:7] offset:384
.Lf_27:
	s_or_b64 exec, exec, s[2:3]
	v_and_b32_e32 v2, 0x3f0, v116
	v_add_u32_e32 v166, 0, v2
	s_waitcnt vmcnt(0)
	ds_write_b128 v39, v[66:69] offset:32768
	ds_write_b128 v39, v[70:73] offset:32784
	ds_write_b128 v39, v[74:77] offset:32800
	ds_write_b128 v39, v[78:81] offset:32816
	s_waitcnt lgkmcnt(0)
	s_barrier
	v_and_b32_e32 v167, 31, v0
	v_lshl_or_b32 v167, s51, 5, v167
	s_mul_i32 s38, s33, 0x1800
	v_add_u32_e32 v2, s38, v167
	v_lshlrev_b32_e32 v2, 5, v2
	v_bfe_u32 v3, v0, 5, 1
	v_lshl_add_u32 v2, v3, 4, v2
	s_mov_b32 s44, s16
	s_mov_b32 s45, s17
	global_load_dwordx4 v[102:105], v2, s[44:45]
	s_add_u32 s44, s44, 0x3000
	s_addc_u32 s45, s45, 0
	global_load_dwordx4 v[106:109], v2, s[44:45]
	s_add_u32 s44, s44, 0x3000
	s_addc_u32 s45, s45, 0
	global_load_dwordx4 v[110:113], v2, s[44:45]
	s_add_u32 s44, s44, 0x3000
	s_addc_u32 s45, s45, 0
	global_load_dwordx4 v[114:117], v2, s[44:45]
	s_add_u32 s44, s44, 0x3000
	s_addc_u32 s45, s45, 0
	global_load_dwordx4 v[118:121], v2, s[44:45]
	s_add_u32 s44, s44, 0x3000
	s_addc_u32 s45, s45, 0
	global_load_dwordx4 v[122:125], v2, s[44:45]
	s_add_u32 s44, s44, 0x3000
	s_addc_u32 s45, s45, 0
	global_load_dwordx4 v[126:129], v2, s[44:45]
	s_add_u32 s44, s44, 0x3000
	s_addc_u32 s45, s45, 0
	global_load_dwordx4 v[130:133], v2, s[44:45]
	s_add_u32 s44, s44, 0x3000
	s_addc_u32 s45, s45, 0
	global_load_dwordx4 v[134:137], v2, s[44:45]
	s_add_u32 s44, s44, 0x3000
	s_addc_u32 s45, s45, 0
	global_load_dwordx4 v[138:141], v2, s[44:45]
	s_add_u32 s44, s44, 0x3000
	s_addc_u32 s45, s45, 0
	global_load_dwordx4 v[142:145], v2, s[44:45]
	s_add_u32 s44, s44, 0x3000
	s_addc_u32 s45, s45, 0
	global_load_dwordx4 v[146:149], v2, s[44:45]
	s_add_u32 s44, s44, 0x3000
	s_addc_u32 s45, s45, 0
	global_load_dwordx4 v[150:153], v2, s[44:45]
	s_add_u32 s44, s44, 0x3000
	s_addc_u32 s45, s45, 0
	global_load_dwordx4 v[154:157], v2, s[44:45]
	s_add_u32 s44, s44, 0x3000
	s_addc_u32 s45, s45, 0
	global_load_dwordx4 v[158:161], v2, s[44:45]
	s_add_u32 s44, s44, 0x3000
	s_addc_u32 s45, s45, 0
	global_load_dwordx4 v[162:165], v2, s[44:45]
	v_mul_u32_u24_e32 v1, 0xc40, v3
	v_lshl_add_u32 v1, v167, 1, v1
	v_add_u32_e32 v1, 0x18000, v1
	v_mov_b32_e32 v90, 0
	v_mov_b32_e32 v91, 0
	v_mov_b32_e32 v92, 0
	v_mov_b32_e32 v93, 0
	v_mov_b32_e32 v94, 0
	v_mov_b32_e32 v95, 0
	v_mov_b32_e32 v96, 0
	v_mov_b32_e32 v97, 0
	v_mov_b32_e32 v98, 0
	v_mov_b32_e32 v99, 0
	v_mov_b32_e32 v100, 0
	v_mov_b32_e32 v101, 0
	ds_read_b128 v[46:49], v166 offset:2048
	ds_read_b128 v[14:17], v166 offset:0
	ds_read_b128 v[30:33], v166 offset:1024
	ds_read_b128 v[62:65], v166 offset:3072
	s_waitcnt vmcnt(14) lgkmcnt(3)
	v_mfma_f32_32x32x16_f16 v[34:49], v[46:49], v[106:109], 0
	s_waitcnt lgkmcnt(2)
	v_mfma_f32_32x32x16_f16 v[2:17], v[14:17], v[102:105], 0
	s_waitcnt lgkmcnt(1)
	v_mfma_f32_32x32x16_f16 v[18:33], v[30:33], v[102:105], 0
	s_waitcnt lgkmcnt(0)
	v_mfma_f32_32x32x16_f16 v[50:65], v[62:65], v[106:109], 0
	s_lshl_b32 s22, s42, 2
	s_cmpk_lt_u32 s49, 0x100
	s_cselect_b32 s20, s14, s10
	s_cselect_b32 s21, s15, s11
	s_cselect_b32 s22, s22, 0
	s_cselect_b32 s23, 0xff, 15
	v_and_b32_e32 v66, s23, v0
	v_lshlrev_b32_e32 v66, 4, v66
	v_add_u32_e32 v66, s22, v66
	global_load_dwordx4 v[102:105], v66, s[20:21]
	s_nop 7
	ds_read_b128 v[46:49], v166 offset:6144
	ds_read_b128 v[14:17], v166 offset:4096
	ds_read_b128 v[30:33], v166 offset:5120
	ds_read_b128 v[62:65], v166 offset:7168
	v_pk_mul_f32 v[66:67], v[34:35], v[18:19]
	v_pk_mul_f32 v[68:69], v[36:37], v[20:21]
	v_pk_mul_f32 v[70:71], v[38:39], v[22:23]
	v_pk_mul_f32 v[72:73], v[40:41], v[24:25]
	v_pk_mul_f32 v[74:75], v[42:43], v[26:27]
	v_pk_mul_f32 v[76:77], v[44:45], v[28:29]
	s_waitcnt vmcnt(13) lgkmcnt(3)
	v_mfma_f32_32x32x16_f16 v[34:49], v[46:49], v[114:117], 0
	v_pk_fma_f32 v[66:67], v[2:3], v[50:51], v[66:67]
	v_pk_fma_f32 v[68:69], v[4:5], v[52:53], v[68:69]
	v_pk_fma_f32 v[70:71], v[6:7], v[54:55], v[70:71]
	v_pk_fma_f32 v[72:73], v[8:9], v[56:57], v[72:73]
	v_pk_fma_f32 v[74:75], v[10:11], v[58:59], v[74:75]
	v_pk_fma_f32 v[76:77], v[12:13], v[60:61], v[76:77]
	s_waitcnt lgkmcnt(2)
	v_mfma_f32_32x32x16_f16 v[2:17], v[14:17], v[110:113], 0
	v_pk_mul_f32 v[78:79], v[18:19], v[50:51]
	v_pk_mul_f32 v[80:81], v[20:21], v[52:53]
	v_pk_mul_f32 v[82:83], v[22:23], v[54:55]
	v_pk_mul_f32 v[84:85], v[24:25], v[56:57]
	v_pk_mul_f32 v[86:87], v[26:27], v[58:59]
	v_pk_mul_f32 v[88:89], v[28:29], v[60:61]
	s_waitcnt lgkmcnt(1)
	v_mfma_f32_32x32x16_f16 v[18:33], v[30:33], v[110:113], 0
	s_waitcnt lgkmcnt(0)
	v_mfma_f32_32x32x16_f16 v[50:65], v[62:65], v[114:117], 0
	v_rcp_f32_e32 v78, v78
	v_rcp_f32_e32 v79, v79
	v_rcp_f32_e32 v80, v80
	v_rcp_f32_e32 v81, v81
	v_rcp_f32_e32 v82, v82
	v_rcp_f32_e32 v83, v83
	v_rcp_f32_e32 v84, v84
	v_rcp_f32_e32 v85, v85
	v_rcp_f32_e32 v86, v86
	v_rcp_f32_e32 v87, v87
	v_rcp_f32_e32 v88, v88
	v_rcp_f32_e32 v89, v89
	v_pk_fma_f32 v[90:91], v[66:67], v[78:79], v[90:91]
	v_pk_fma_f32 v[92:93], v[68:69], v[80:81], v[92:93]
	v_pk_fma_f32 v[94:95], v[70:71], v[82:83], v[94:95]
	v_pk_fma_f32 v[96:97], v[72:73], v[84:85], v[96:97]
	v_pk_fma_f32 v[98:99], v[74:75], v[86:87], v[98:99]
	v_pk_fma_f32 v[100:101], v[76:77], v[88:89], v[100:101]
	ds_read_b128 v[46:49], v166 offset:10240
	ds_read_b128 v[14:17], v166 offset:8192
	ds_read_b128 v[30:33], v166 offset:9216
	ds_read_b128 v[62:65], v166 offset:11264
	v_pk_mul_f32 v[66:67], v[34:35], v[18:19]
	v_pk_mul_f32 v[68:69], v[36:37], v[20:21]
	v_pk_mul_f32 v[70:71], v[38:39], v[22:23]
	v_pk_mul_f32 v[72:73], v[40:41], v[24:25]
	v_pk_mul_f32 v[74:75], v[42:43], v[26:27]
	v_pk_mul_f32 v[76:77], v[44:45], v[28:29]
	s_waitcnt vmcnt(11) lgkmcnt(3)
	v_mfma_f32_32x32x16_f16 v[34:49], v[46:49], v[122:125], 0
	v_pk_fma_f32 v[66:67], v[2:3], v[50:51], v[66:67]
	v_pk_fma_f32 v[68:69], v[4:5], v[52:53], v[68:69]
	v_pk_fma_f32 v[70:71], v[6:7], v[54:55], v[70:71]
	v_pk_fma_f32 v[72:73], v[8:9], v[56:57], v[72:73]
	v_pk_fma_f32 v[74:75], v[10:11], v[58:59], v[74:75]
	v_pk_fma_f32 v[76:77], v[12:13], v[60:61], v[76:77]
	s_waitcnt lgkmcnt(2)
	v_mfma_f32_32x32x16_f16 v[2:17], v[14:17], v[118:121], 0
	v_pk_mul_f32 v[78:79], v[18:19], v[50:51]
	v_pk_mul_f32 v[80:81], v[20:21], v[52:53]
	v_pk_mul_f32 v[82:83], v[22:23], v[54:55]
	v_pk_mul_f32 v[84:85], v[24:25], v[56:57]
	v_pk_mul_f32 v[86:87], v[26:27], v[58:59]
	v_pk_mul_f32 v[88:89], v[28:29], v[60:61]
	s_waitcnt lgkmcnt(1)
	v_mfma_f32_32x32x16_f16 v[18:33], v[30:33], v[118:121], 0
	s_waitcnt lgkmcnt(0)
	v_mfma_f32_32x32x16_f16 v[50:65], v[62:65], v[122:125], 0
	v_rcp_f32_e32 v78, v78
	v_rcp_f32_e32 v79, v79
	v_rcp_f32_e32 v80, v80
	v_rcp_f32_e32 v81, v81
	v_rcp_f32_e32 v82, v82
	v_rcp_f32_e32 v83, v83
	v_rcp_f32_e32 v84, v84
	v_rcp_f32_e32 v85, v85
	v_rcp_f32_e32 v86, v86
	v_rcp_f32_e32 v87, v87
	v_rcp_f32_e32 v88, v88
	v_rcp_f32_e32 v89, v89
	v_pk_fma_f32 v[90:91], v[66:67], v[78:79], v[90:91]
	v_pk_fma_f32 v[92:93], v[68:69], v[80:81], v[92:93]
	v_pk_fma_f32 v[94:95], v[70:71], v[82:83], v[94:95]
	v_pk_fma_f32 v[96:97], v[72:73], v[84:85], v[96:97]
	v_pk_fma_f32 v[98:99], v[74:75], v[86:87], v[98:99]
	v_pk_fma_f32 v[100:101], v[76:77], v[88:89], v[100:101]
	ds_read_b128 v[46:49], v166 offset:14336
	ds_read_b128 v[14:17], v166 offset:12288
	ds_read_b128 v[30:33], v166 offset:13312
	ds_read_b128 v[62:65], v166 offset:15360
	v_pk_mul_f32 v[66:67], v[34:35], v[18:19]
	v_pk_mul_f32 v[68:69], v[36:37], v[20:21]
	v_pk_mul_f32 v[70:71], v[38:39], v[22:23]
	v_pk_mul_f32 v[72:73], v[40:41], v[24:25]
	v_pk_mul_f32 v[74:75], v[42:43], v[26:27]
	v_pk_mul_f32 v[76:77], v[44:45], v[28:29]
	s_waitcnt vmcnt(9) lgkmcnt(3)
	v_mfma_f32_32x32x16_f16 v[34:49], v[46:49], v[130:133], 0
	v_pk_fma_f32 v[66:67], v[2:3], v[50:51], v[66:67]
	v_pk_fma_f32 v[68:69], v[4:5], v[52:53], v[68:69]
	v_pk_fma_f32 v[70:71], v[6:7], v[54:55], v[70:71]
	v_pk_fma_f32 v[72:73], v[8:9], v[56:57], v[72:73]
	v_pk_fma_f32 v[74:75], v[10:11], v[58:59], v[74:75]
	v_pk_fma_f32 v[76:77], v[12:13], v[60:61], v[76:77]
	s_waitcnt lgkmcnt(2)
	v_mfma_f32_32x32x16_f16 v[2:17], v[14:17], v[126:129], 0
	v_pk_mul_f32 v[78:79], v[18:19], v[50:51]
	v_pk_mul_f32 v[80:81], v[20:21], v[52:53]
	v_pk_mul_f32 v[82:83], v[22:23], v[54:55]
	v_pk_mul_f32 v[84:85], v[24:25], v[56:57]
	v_pk_mul_f32 v[86:87], v[26:27], v[58:59]
	v_pk_mul_f32 v[88:89], v[28:29], v[60:61]
	s_waitcnt lgkmcnt(1)
	v_mfma_f32_32x32x16_f16 v[18:33], v[30:33], v[126:129], 0
	s_waitcnt lgkmcnt(0)
	v_mfma_f32_32x32x16_f16 v[50:65], v[62:65], v[130:133], 0
	v_rcp_f32_e32 v78, v78
	v_rcp_f32_e32 v79, v79
	v_rcp_f32_e32 v80, v80
	v_rcp_f32_e32 v81, v81
	v_rcp_f32_e32 v82, v82
	v_rcp_f32_e32 v83, v83
	v_rcp_f32_e32 v84, v84
	v_rcp_f32_e32 v85, v85
	v_rcp_f32_e32 v86, v86
	v_rcp_f32_e32 v87, v87
	v_rcp_f32_e32 v88, v88
	v_rcp_f32_e32 v89, v89
	v_pk_fma_f32 v[90:91], v[66:67], v[78:79], v[90:91]
	v_pk_fma_f32 v[92:93], v[68:69], v[80:81], v[92:93]
	v_pk_fma_f32 v[94:95], v[70:71], v[82:83], v[94:95]
	v_pk_fma_f32 v[96:97], v[72:73], v[84:85], v[96:97]
	v_pk_fma_f32 v[98:99], v[74:75], v[86:87], v[98:99]
	v_pk_fma_f32 v[100:101], v[76:77], v[88:89], v[100:101]
	ds_read_b128 v[46:49], v166 offset:18432
	ds_read_b128 v[14:17], v166 offset:16384
	ds_read_b128 v[30:33], v166 offset:17408
	ds_read_b128 v[62:65], v166 offset:19456
	v_pk_mul_f32 v[66:67], v[34:35], v[18:19]
	v_pk_mul_f32 v[68:69], v[36:37], v[20:21]
	v_pk_mul_f32 v[70:71], v[38:39], v[22:23]
	v_pk_mul_f32 v[72:73], v[40:41], v[24:25]
	v_pk_mul_f32 v[74:75], v[42:43], v[26:27]
	v_pk_mul_f32 v[76:77], v[44:45], v[28:29]
	s_waitcnt vmcnt(7) lgkmcnt(3)
	v_mfma_f32_32x32x16_f16 v[34:49], v[46:49], v[138:141], 0
	v_pk_fma_f32 v[66:67], v[2:3], v[50:51], v[66:67]
	v_pk_fma_f32 v[68:69], v[4:5], v[52:53], v[68:69]
	v_pk_fma_f32 v[70:71], v[6:7], v[54:55], v[70:71]
	v_pk_fma_f32 v[72:73], v[8:9], v[56:57], v[72:73]
	v_pk_fma_f32 v[74:75], v[10:11], v[58:59], v[74:75]
	v_pk_fma_f32 v[76:77], v[12:13], v[60:61], v[76:77]
	s_waitcnt lgkmcnt(2)
	v_mfma_f32_32x32x16_f16 v[2:17], v[14:17], v[134:137], 0
	v_pk_mul_f32 v[78:79], v[18:19], v[50:51]
	v_pk_mul_f32 v[80:81], v[20:21], v[52:53]
	v_pk_mul_f32 v[82:83], v[22:23], v[54:55]
	v_pk_mul_f32 v[84:85], v[24:25], v[56:57]
	v_pk_mul_f32 v[86:87], v[26:27], v[58:59]
	v_pk_mul_f32 v[88:89], v[28:29], v[60:61]
	s_waitcnt lgkmcnt(1)
	v_mfma_f32_32x32x16_f16 v[18:33], v[30:33], v[134:137], 0
	s_waitcnt lgkmcnt(0)
	v_mfma_f32_32x32x16_f16 v[50:65], v[62:65], v[138:141], 0
	v_rcp_f32_e32 v78, v78
	v_rcp_f32_e32 v79, v79
	v_rcp_f32_e32 v80, v80
	v_rcp_f32_e32 v81, v81
	v_rcp_f32_e32 v82, v82
	v_rcp_f32_e32 v83, v83
	v_rcp_f32_e32 v84, v84
	v_rcp_f32_e32 v85, v85
	v_rcp_f32_e32 v86, v86
	v_rcp_f32_e32 v87, v87
	v_rcp_f32_e32 v88, v88
	v_rcp_f32_e32 v89, v89
	v_pk_fma_f32 v[90:91], v[66:67], v[78:79], v[90:91]
	v_pk_fma_f32 v[92:93], v[68:69], v[80:81], v[92:93]
	v_pk_fma_f32 v[94:95], v[70:71], v[82:83], v[94:95]
	v_pk_fma_f32 v[96:97], v[72:73], v[84:85], v[96:97]
	v_pk_fma_f32 v[98:99], v[74:75], v[86:87], v[98:99]
	v_pk_fma_f32 v[100:101], v[76:77], v[88:89], v[100:101]
	ds_read_b128 v[46:49], v166 offset:22528
	ds_read_b128 v[14:17], v166 offset:20480
	ds_read_b128 v[30:33], v166 offset:21504
	ds_read_b128 v[62:65], v166 offset:23552
	v_pk_mul_f32 v[66:67], v[34:35], v[18:19]
	v_pk_mul_f32 v[68:69], v[36:37], v[20:21]
	v_pk_mul_f32 v[70:71], v[38:39], v[22:23]
	v_pk_mul_f32 v[72:73], v[40:41], v[24:25]
	v_pk_mul_f32 v[74:75], v[42:43], v[26:27]
	v_pk_mul_f32 v[76:77], v[44:45], v[28:29]
	s_waitcnt vmcnt(5) lgkmcnt(3)
	v_mfma_f32_32x32x16_f16 v[34:49], v[46:49], v[146:149], 0
	v_pk_fma_f32 v[66:67], v[2:3], v[50:51], v[66:67]
	v_pk_fma_f32 v[68:69], v[4:5], v[52:53], v[68:69]
	v_pk_fma_f32 v[70:71], v[6:7], v[54:55], v[70:71]
	v_pk_fma_f32 v[72:73], v[8:9], v[56:57], v[72:73]
	v_pk_fma_f32 v[74:75], v[10:11], v[58:59], v[74:75]
	v_pk_fma_f32 v[76:77], v[12:13], v[60:61], v[76:77]
	s_waitcnt lgkmcnt(2)
	v_mfma_f32_32x32x16_f16 v[2:17], v[14:17], v[142:145], 0
	v_pk_mul_f32 v[78:79], v[18:19], v[50:51]
	v_pk_mul_f32 v[80:81], v[20:21], v[52:53]
	v_pk_mul_f32 v[82:83], v[22:23], v[54:55]
	v_pk_mul_f32 v[84:85], v[24:25], v[56:57]
	v_pk_mul_f32 v[86:87], v[26:27], v[58:59]
	v_pk_mul_f32 v[88:89], v[28:29], v[60:61]
	s_waitcnt lgkmcnt(1)
	v_mfma_f32_32x32x16_f16 v[18:33], v[30:33], v[142:145], 0
	s_waitcnt lgkmcnt(0)
	v_mfma_f32_32x32x16_f16 v[50:65], v[62:65], v[146:149], 0
	v_rcp_f32_e32 v78, v78
	v_rcp_f32_e32 v79, v79
	v_rcp_f32_e32 v80, v80
	v_rcp_f32_e32 v81, v81
	v_rcp_f32_e32 v82, v82
	v_rcp_f32_e32 v83, v83
	v_rcp_f32_e32 v84, v84
	v_rcp_f32_e32 v85, v85
	v_rcp_f32_e32 v86, v86
	v_rcp_f32_e32 v87, v87
	v_rcp_f32_e32 v88, v88
	v_rcp_f32_e32 v89, v89
	v_pk_fma_f32 v[90:91], v[66:67], v[78:79], v[90:91]
	v_pk_fma_f32 v[92:93], v[68:69], v[80:81], v[92:93]
	v_pk_fma_f32 v[94:95], v[70:71], v[82:83], v[94:95]
	v_pk_fma_f32 v[96:97], v[72:73], v[84:85], v[96:97]
	v_pk_fma_f32 v[98:99], v[74:75], v[86:87], v[98:99]
	v_pk_fma_f32 v[100:101], v[76:77], v[88:89], v[100:101]
	ds_read_b128 v[46:49], v166 offset:26624
	ds_read_b128 v[14:17], v166 offset:24576
	ds_read_b128 v[30:33], v166 offset:25600
	ds_read_b128 v[62:65], v166 offset:27648
	v_pk_mul_f32 v[66:67], v[34:35], v[18:19]
	v_pk_mul_f32 v[68:69], v[36:37], v[20:21]
	v_pk_mul_f32 v[70:71], v[38:39], v[22:23]
	v_pk_mul_f32 v[72:73], v[40:41], v[24:25]
	v_pk_mul_f32 v[74:75], v[42:43], v[26:27]
	v_pk_mul_f32 v[76:77], v[44:45], v[28:29]
	s_waitcnt vmcnt(3) lgkmcnt(3)
	v_mfma_f32_32x32x16_f16 v[34:49], v[46:49], v[154:157], 0
	v_pk_fma_f32 v[66:67], v[2:3], v[50:51], v[66:67]
	v_pk_fma_f32 v[68:69], v[4:5], v[52:53], v[68:69]
	v_pk_fma_f32 v[70:71], v[6:7], v[54:55], v[70:71]
	v_pk_fma_f32 v[72:73], v[8:9], v[56:57], v[72:73]
	v_pk_fma_f32 v[74:75], v[10:11], v[58:59], v[74:75]
	v_pk_fma_f32 v[76:77], v[12:13], v[60:61], v[76:77]
	s_waitcnt lgkmcnt(2)
	v_mfma_f32_32x32x16_f16 v[2:17], v[14:17], v[150:153], 0
	v_pk_mul_f32 v[78:79], v[18:19], v[50:51]
	v_pk_mul_f32 v[80:81], v[20:21], v[52:53]
	v_pk_mul_f32 v[82:83], v[22:23], v[54:55]
	v_pk_mul_f32 v[84:85], v[24:25], v[56:57]
	v_pk_mul_f32 v[86:87], v[26:27], v[58:59]
	v_pk_mul_f32 v[88:89], v[28:29], v[60:61]
	s_waitcnt lgkmcnt(1)
	v_mfma_f32_32x32x16_f16 v[18:33], v[30:33], v[150:153], 0
	s_waitcnt lgkmcnt(0)
	v_mfma_f32_32x32x16_f16 v[50:65], v[62:65], v[154:157], 0
	v_rcp_f32_e32 v78, v78
	v_rcp_f32_e32 v79, v79
	v_rcp_f32_e32 v80, v80
	v_rcp_f32_e32 v81, v81
	v_rcp_f32_e32 v82, v82
	v_rcp_f32_e32 v83, v83
	v_rcp_f32_e32 v84, v84
	v_rcp_f32_e32 v85, v85
	v_rcp_f32_e32 v86, v86
	v_rcp_f32_e32 v87, v87
	v_rcp_f32_e32 v88, v88
	v_rcp_f32_e32 v89, v89
	v_pk_fma_f32 v[90:91], v[66:67], v[78:79], v[90:91]
	v_pk_fma_f32 v[92:93], v[68:69], v[80:81], v[92:93]
	v_pk_fma_f32 v[94:95], v[70:71], v[82:83], v[94:95]
	v_pk_fma_f32 v[96:97], v[72:73], v[84:85], v[96:97]
	v_pk_fma_f32 v[98:99], v[74:75], v[86:87], v[98:99]
	v_pk_fma_f32 v[100:101], v[76:77], v[88:89], v[100:101]
	ds_read_b128 v[46:49], v166 offset:30720
	ds_read_b128 v[14:17], v166 offset:28672
	ds_read_b128 v[30:33], v166 offset:29696
	ds_read_b128 v[62:65], v166 offset:31744
	v_pk_mul_f32 v[66:67], v[34:35], v[18:19]
	v_pk_mul_f32 v[68:69], v[36:37], v[20:21]
	v_pk_mul_f32 v[70:71], v[38:39], v[22:23]
	v_pk_mul_f32 v[72:73], v[40:41], v[24:25]
	v_pk_mul_f32 v[74:75], v[42:43], v[26:27]
	v_pk_mul_f32 v[76:77], v[44:45], v[28:29]
	s_waitcnt vmcnt(1) lgkmcnt(3)
	v_mfma_f32_32x32x16_f16 v[34:49], v[46:49], v[162:165], 0
	v_pk_fma_f32 v[66:67], v[2:3], v[50:51], v[66:67]
	v_pk_fma_f32 v[68:69], v[4:5], v[52:53], v[68:69]
	v_pk_fma_f32 v[70:71], v[6:7], v[54:55], v[70:71]
	v_pk_fma_f32 v[72:73], v[8:9], v[56:57], v[72:73]
	v_pk_fma_f32 v[74:75], v[10:11], v[58:59], v[74:75]
	v_pk_fma_f32 v[76:77], v[12:13], v[60:61], v[76:77]
	s_waitcnt lgkmcnt(2)
	v_mfma_f32_32x32x16_f16 v[2:17], v[14:17], v[158:161], 0
	v_pk_mul_f32 v[78:79], v[18:19], v[50:51]
	v_pk_mul_f32 v[80:81], v[20:21], v[52:53]
	v_pk_mul_f32 v[82:83], v[22:23], v[54:55]
	v_pk_mul_f32 v[84:85], v[24:25], v[56:57]
	v_pk_mul_f32 v[86:87], v[26:27], v[58:59]
	v_pk_mul_f32 v[88:89], v[28:29], v[60:61]
	s_waitcnt lgkmcnt(1)
	v_mfma_f32_32x32x16_f16 v[18:33], v[30:33], v[158:161], 0
	s_waitcnt lgkmcnt(0)
	v_mfma_f32_32x32x16_f16 v[50:65], v[62:65], v[162:165], 0
	v_rcp_f32_e32 v78, v78
	v_rcp_f32_e32 v79, v79
	v_rcp_f32_e32 v80, v80
	v_rcp_f32_e32 v81, v81
	v_rcp_f32_e32 v82, v82
	v_rcp_f32_e32 v83, v83
	v_rcp_f32_e32 v84, v84
	v_rcp_f32_e32 v85, v85
	v_rcp_f32_e32 v86, v86
	v_rcp_f32_e32 v87, v87
	v_rcp_f32_e32 v88, v88
	v_rcp_f32_e32 v89, v89
	v_pk_fma_f32 v[90:91], v[66:67], v[78:79], v[90:91]
	v_pk_fma_f32 v[92:93], v[68:69], v[80:81], v[92:93]
	v_pk_fma_f32 v[94:95], v[70:71], v[82:83], v[94:95]
	v_pk_fma_f32 v[96:97], v[72:73], v[84:85], v[96:97]
	v_pk_fma_f32 v[98:99], v[74:75], v[86:87], v[98:99]
	v_pk_fma_f32 v[100:101], v[76:77], v[88:89], v[100:101]
	v_pk_mul_f32 v[66:67], v[34:35], v[18:19]
	v_pk_mul_f32 v[68:69], v[36:37], v[20:21]
	v_pk_mul_f32 v[70:71], v[38:39], v[22:23]
	v_pk_mul_f32 v[72:73], v[40:41], v[24:25]
	v_pk_mul_f32 v[74:75], v[42:43], v[26:27]
	v_pk_mul_f32 v[76:77], v[44:45], v[28:29]
	v_pk_fma_f32 v[66:67], v[2:3], v[50:51], v[66:67]
	v_pk_fma_f32 v[68:69], v[4:5], v[52:53], v[68:69]
	v_pk_fma_f32 v[70:71], v[6:7], v[54:55], v[70:71]
	v_pk_fma_f32 v[72:73], v[8:9], v[56:57], v[72:73]
	v_pk_fma_f32 v[74:75], v[10:11], v[58:59], v[74:75]
	v_pk_fma_f32 v[76:77], v[12:13], v[60:61], v[76:77]
	v_pk_mul_f32 v[78:79], v[18:19], v[50:51]
	v_pk_mul_f32 v[80:81], v[20:21], v[52:53]
	v_pk_mul_f32 v[82:83], v[22:23], v[54:55]
	v_pk_mul_f32 v[84:85], v[24:25], v[56:57]
	v_pk_mul_f32 v[86:87], v[26:27], v[58:59]
	v_pk_mul_f32 v[88:89], v[28:29], v[60:61]
	v_rcp_f32_e32 v78, v78
	v_rcp_f32_e32 v79, v79
	v_rcp_f32_e32 v80, v80
	v_rcp_f32_e32 v81, v81
	v_rcp_f32_e32 v82, v82
	v_rcp_f32_e32 v83, v83
	v_rcp_f32_e32 v84, v84
	v_rcp_f32_e32 v85, v85
	v_rcp_f32_e32 v86, v86
	v_rcp_f32_e32 v87, v87
	v_rcp_f32_e32 v88, v88
	v_rcp_f32_e32 v89, v89
	v_pk_fma_f32 v[90:91], v[66:67], v[78:79], v[90:91]
	v_pk_fma_f32 v[92:93], v[68:69], v[80:81], v[92:93]
	v_pk_fma_f32 v[94:95], v[70:71], v[82:83], v[94:95]
	v_pk_fma_f32 v[96:97], v[72:73], v[84:85], v[96:97]
	v_pk_fma_f32 v[98:99], v[74:75], v[86:87], v[98:99]
	v_pk_fma_f32 v[100:101], v[76:77], v[88:89], v[100:101]
	v_fma_f32 v66, v90, -2.0, s28
	v_subrev_f32_e32 v66, s29, v66
	v_mul_f32_e32 v66, 0x3fb8aa3b, v66
	v_exp_f32_e32 v66, v66
	v_fma_f32 v67, v91, -2.0, s28
	v_subrev_f32_e32 v67, s29, v67
	v_mul_f32_e32 v67, 0x3fb8aa3b, v67
	v_exp_f32_e32 v67, v67
	v_fma_f32 v68, v92, -2.0, s28
	v_subrev_f32_e32 v68, s29, v68
	v_mul_f32_e32 v68, 0x3fb8aa3b, v68
	v_exp_f32_e32 v68, v68
	v_fma_f32 v69, v93, -2.0, s28
	v_subrev_f32_e32 v69, s29, v69
	v_mul_f32_e32 v69, 0x3fb8aa3b, v69
	v_exp_f32_e32 v69, v69
	v_fma_f32 v70, v94, -2.0, s28
	v_subrev_f32_e32 v70, s29, v70
	v_mul_f32_e32 v70, 0x3fb8aa3b, v70
	v_exp_f32_e32 v70, v70
	v_fma_f32 v71, v95, -2.0, s28
	v_subrev_f32_e32 v71, s29, v71
	v_mul_f32_e32 v71, 0x3fb8aa3b, v71
	v_exp_f32_e32 v71, v71
	v_fma_f32 v72, v96, -2.0, s28
	v_subrev_f32_e32 v72, s29, v72
	v_mul_f32_e32 v72, 0x3fb8aa3b, v72
	v_exp_f32_e32 v72, v72
	v_fma_f32 v73, v97, -2.0, s28
	v_subrev_f32_e32 v73, s29, v73
	v_mul_f32_e32 v73, 0x3fb8aa3b, v73
	v_exp_f32_e32 v73, v73
	v_fma_f32 v74, v98, -2.0, s28
	v_subrev_f32_e32 v74, s29, v74
	v_mul_f32_e32 v74, 0x3fb8aa3b, v74
	v_exp_f32_e32 v74, v74
	v_fma_f32 v75, v99, -2.0, s28
	v_subrev_f32_e32 v75, s29, v75
	v_mul_f32_e32 v75, 0x3fb8aa3b, v75
	v_exp_f32_e32 v75, v75
	v_fma_f32 v76, v100, -2.0, s28
	v_subrev_f32_e32 v76, s29, v76
	v_mul_f32_e32 v76, 0x3fb8aa3b, v76
	v_exp_f32_e32 v76, v76
	v_fma_f32 v77, v101, -2.0, s28
	v_subrev_f32_e32 v77, s29, v77
	v_mul_f32_e32 v77, 0x3fb8aa3b, v77
	v_exp_f32_e32 v77, v77
	s_nop 0
	v_cvt_f16_f32_e32 v66, v66
	v_cvt_f16_f32_e32 v67, v67
	v_cvt_f16_f32_e32 v68, v68
	v_cvt_f16_f32_e32 v69, v69
	v_cvt_f16_f32_e32 v70, v70
	v_cvt_f16_f32_e32 v71, v71
	v_cvt_f16_f32_e32 v72, v72
	v_cvt_f16_f32_e32 v73, v73
	v_cvt_f16_f32_e32 v74, v74
	v_cvt_f16_f32_e32 v75, v75
	v_cvt_f16_f32_e32 v76, v76
	v_cvt_f16_f32_e32 v77, v77
	ds_write_b16 v1, v66
	ds_write_b16 v1, v67 offset:784
	ds_write_b16 v1, v68 offset:1568
	ds_write_b16 v1, v69 offset:2352
	ds_write_b16 v1, v70 offset:6272
	ds_write_b16 v1, v71 offset:7056
	ds_write_b16 v1, v72 offset:7840
	ds_write_b16 v1, v73 offset:8624
	ds_write_b16 v1, v74 offset:12544
	ds_write_b16 v1, v75 offset:13328
	ds_write_b16 v1, v76 offset:14112
	ds_write_b16 v1, v77 offset:14896
	s_cmpk_gt_u32 s49, 0xff
	s_cbranch_scc1 .Lf_wo_done
	s_waitcnt vmcnt(0)
	v_cvt_f16_f32_e32 v2, v102
	v_cvt_f16_f32_e32 v5, v105
	v_cvt_pk_f16_f32 v3, v103, v104
	v_pack_b32_f16 v2, v2, v3
	v_alignbit_b32 v3, v5, v3, 16
	v_and_b32_e32 v6, 0xff, v0
	v_lshlrev_b32_e32 v6, 3, v6
	s_lshl_b32 s22, s42, 1
	v_add_u32_e32 v6, s22, v6
	global_store_dwordx2 v6, v[2:3], s[18:19]
.Lf_wo_done:
	s_waitcnt lgkmcnt(0)
	s_barrier
	s_cmpk_gt_u32 s49, 0x1ff
	s_cbranch_scc0 .Lf_pv
	s_endpgm
.Lf_pv:
	s_lshr_b32 s2, s49, 4
	s_and_b32 s2, s2, 16
	s_and_b32 s4, s51, 3
	v_and_b32_e32 v62, 15, v0
	v_or_b32_e32 v1, s2, v62
	v_mul_u32_u24_e32 v1, 0x310, v1
	v_and_b32_e32 v50, 48, v0
	s_mov_b32 s6, 0x18000
	v_add3_u32 v1, s6, v1, v50
	s_lshl_b32 s5, s4, 4
	v_or_b32_e32 v51, s5, v62
	v_mul_u32_u24_e32 v51, 0x320, v51
	s_mov_b32 s7, 0x8000
	v_add3_u32 v51, s7, v51, v50
	v_mov_b32_e32 v74, 0x3c003c00
	v_mov_b32_e32 v75, v74
	v_mov_b32_e32 v76, v74
	v_mov_b32_e32 v77, v74
	ds_read_b128 v[2:5], v1
	ds_read_b128 v[102:105], v51
	ds_read_b128 v[6:9], v1 offset:64
	ds_read_b128 v[106:109], v51 offset:64
	ds_read_b128 v[10:13], v1 offset:128
	ds_read_b128 v[110:113], v51 offset:128
	ds_read_b128 v[14:17], v1 offset:192
	ds_read_b128 v[114:117], v51 offset:192
	ds_read_b128 v[18:21], v1 offset:256
	ds_read_b128 v[118:121], v51 offset:256
	ds_read_b128 v[22:25], v1 offset:320
	ds_read_b128 v[122:125], v51 offset:320
	ds_read_b128 v[26:29], v1 offset:384
	ds_read_b128 v[126:129], v51 offset:384
	s_waitcnt lgkmcnt(12)
	v_mfma_f32_16x16x32_f16 v[66:69], v[2:5], v[102:105], 0
	v_mfma_f32_16x16x32_f16 v[70:73], v[2:5], v[74:77], 0
	ds_read_b128 v[30:33], v1 offset:448
	ds_read_b128 v[130:133], v51 offset:448
	s_waitcnt lgkmcnt(12)
	v_mfma_f32_16x16x32_f16 v[66:69], v[6:9], v[106:109], v[66:69]
	v_mfma_f32_16x16x32_f16 v[70:73], v[6:9], v[74:77], v[70:73]
	ds_read_b128 v[34:37], v1 offset:512
	ds_read_b128 v[134:137], v51 offset:512
	s_waitcnt lgkmcnt(12)
	v_mfma_f32_16x16x32_f16 v[66:69], v[10:13], v[110:113], v[66:69]
	v_mfma_f32_16x16x32_f16 v[70:73], v[10:13], v[74:77], v[70:73]
	ds_read_b128 v[38:41], v1 offset:576
	ds_read_b128 v[138:141], v51 offset:576
	s_waitcnt lgkmcnt(12)
	v_mfma_f32_16x16x32_f16 v[66:69], v[14:17], v[114:117], v[66:69]
	v_mfma_f32_16x16x32_f16 v[70:73], v[14:17], v[74:77], v[70:73]
	ds_read_b128 v[42:45], v1 offset:640
	ds_read_b128 v[142:145], v51 offset:640
	s_waitcnt lgkmcnt(12)
	v_mfma_f32_16x16x32_f16 v[66:69], v[18:21], v[118:121], v[66:69]
	v_mfma_f32_16x16x32_f16 v[70:73], v[18:21], v[74:77], v[70:73]
	ds_read_b128 v[46:49], v1 offset:704
	ds_read_b128 v[146:149], v51 offset:704
	s_waitcnt lgkmcnt(12)
	v_mfma_f32_16x16x32_f16 v[66:69], v[22:25], v[122:125], v[66:69]
	v_mfma_f32_16x16x32_f16 v[70:73], v[22:25], v[74:77], v[70:73]
	s_waitcnt lgkmcnt(10)
	v_mfma_f32_16x16x32_f16 v[66:69], v[26:29], v[126:129], v[66:69]
	v_mfma_f32_16x16x32_f16 v[70:73], v[26:29], v[74:77], v[70:73]
	s_waitcnt lgkmcnt(8)
	v_mfma_f32_16x16x32_f16 v[66:69], v[30:33], v[130:133], v[66:69]
	v_mfma_f32_16x16x32_f16 v[70:73], v[30:33], v[74:77], v[70:73]
	s_waitcnt lgkmcnt(6)
	v_mfma_f32_16x16x32_f16 v[66:69], v[34:37], v[134:137], v[66:69]
	v_mfma_f32_16x16x32_f16 v[70:73], v[34:37], v[74:77], v[70:73]
	s_waitcnt lgkmcnt(4)
	v_mfma_f32_16x16x32_f16 v[66:69], v[38:41], v[138:141], v[66:69]
	v_mfma_f32_16x16x32_f16 v[70:73], v[38:41], v[74:77], v[70:73]
	s_waitcnt lgkmcnt(2)
	v_mfma_f32_16x16x32_f16 v[66:69], v[42:45], v[142:145], v[66:69]
	v_mfma_f32_16x16x32_f16 v[70:73], v[42:45], v[74:77], v[70:73]
	s_waitcnt lgkmcnt(0)
	v_mfma_f32_16x16x32_f16 v[66:69], v[46:49], v[146:149], v[66:69]
	v_mfma_f32_16x16x32_f16 v[70:73], v[46:49], v[74:77], v[70:73]
	s_lshr_b32 s3, s43, 3
	s_mul_i32 s5, s3, 0x180
	s_add_i32 s5, s5, s41
	v_lshrrev_b32_e32 v12, 2, v0
	v_and_or_b32 v12, v12, 12, s2
	s_lshl_b32 s2, s33, 7
	s_and_b32 s2, s2, 0x380
	s_add_u32 s0, s62, s2
	s_addc_u32 s1, s63, 0
	s_lshl_b32 s2, s4, 5
	s_add_u32 s0, s0, s2
	s_addc_u32 s1, s1, 0
	v_lshlrev_b32_e32 v10, 1, v62
	v_mov_b32_e32 v11, 0
	v_lshl_add_u64 v[8:9], s[0:1], 0, v[10:11]
	s_nop 4
	v_mov_b32_e32 v0, v66
	v_mov_b32_e32 v1, v67
	v_mov_b32_e32 v2, v68
	v_mov_b32_e32 v3, v69
	v_mov_b32_e32 v4, v70
	v_mov_b32_e32 v5, v71
	v_mov_b32_e32 v6, v72
	v_mov_b32_e32 v7, v73
	v_cmp_gt_u32_e64 s[0:1], 24, v12
	s_and_saveexec_b64 s[2:3], s[0:1]
	s_cbranch_execnz .Lf_37
	s_or_b64 exec, exec, s[2:3]
	s_and_saveexec_b64 s[2:3], s[0:1]
	s_cbranch_execnz .Lf_38

	.amdhsa_kernel _Z11attn_kernelPKfS0_PKDF16_S0_S0_S0_S2_PDF16_S3_
		.amdhsa_group_segment_fixed_size 0
		.amdhsa_private_segment_fixed_size 0
		.amdhsa_kernarg_size 72
		.amdhsa_user_sgpr_count 2
		.amdhsa_user_sgpr_dispatch_ptr 0
		.amdhsa_user_sgpr_queue_ptr 0
		.amdhsa_user_sgpr_kernarg_segment_ptr 1
		.amdhsa_user_sgpr_dispatch_id 0
		.amdhsa_user_sgpr_kernarg_preload_length 0
		.amdhsa_user_sgpr_kernarg_preload_offset 0
		.amdhsa_user_sgpr_private_segment_size 0
		.amdhsa_uses_dynamic_stack 0
		.amdhsa_enable_private_segment 0
		.amdhsa_system_sgpr_workgroup_id_x 1
		.amdhsa_system_sgpr_workgroup_id_y 0
		.amdhsa_system_sgpr_workgroup_id_z 0
		.amdhsa_system_sgpr_workgroup_info 0
		.amdhsa_system_vgpr_workitem_id 0
		.amdhsa_next_free_vgpr 168
		.amdhsa_next_free_sgpr 64
		.amdhsa_accum_offset 168
		.amdhsa_reserve_vcc 1
		.amdhsa_float_round_mode_32 0
		.amdhsa_float_round_mode_16_64 0
		.amdhsa_float_denorm_mode_32 3
		.amdhsa_float_denorm_mode_16_64 3
		.amdhsa_dx10_clamp 1
		.amdhsa_ieee_mode 1
		.amdhsa_fp16_overflow 0
		.amdhsa_tg_split 0
		.amdhsa_exception_fp_ieee_invalid_op 0
		.amdhsa_exception_fp_denorm_src 0
		.amdhsa_exception_fp_ieee_div_zero 0
		.amdhsa_exception_fp_ieee_overflow 0
		.amdhsa_exception_fp_ieee_underflow 0
		.amdhsa_exception_fp_ieee_inexact 0
		.amdhsa_exception_int_div_zero 0
	.end_amdhsa_kernel

amdhsa.kernels:
  - .agpr_count:     0
    .args:
      - .actual_access:  read_only
        .address_space:  global
        .offset:         0
        .size:           8
        .value_kind:     global_buffer
      - .actual_access:  read_only
        .address_space:  global
        .offset:         8
        .size:           8
        .value_kind:     global_buffer
      - .actual_access:  read_only
        .address_space:  global
        .offset:         16
        .size:           8
        .value_kind:     global_buffer
      - .actual_access:  read_only
        .address_space:  global
        .offset:         24
        .size:           8
        .value_kind:     global_buffer
      - .address_space:  global
        .offset:         32
        .size:           8
        .value_kind:     global_buffer
      - .actual_access:  read_only
        .address_space:  global
        .offset:         40
        .size:           8
        .value_kind:     global_buffer
      - .address_space:  global
        .offset:         48
        .size:           8
        .value_kind:     global_buffer
      - .actual_access:  read_only
        .address_space:  global
        .offset:         56
        .size:           8
        .value_kind:     global_buffer
      - .address_space:  global
        .offset:         64
        .size:           8
        .value_kind:     global_buffer
      - .address_space:  global
        .offset:         72
        .size:           8
        .value_kind:     global_buffer
      - .address_space:  global
        .offset:         80
        .size:           8
        .value_kind:     global_buffer
      - .address_space:  global
        .offset:         88
        .size:           8
        .value_kind:     global_buffer
      - .address_space:  global
        .offset:         96
        .size:           8
        .value_kind:     global_buffer
      - .actual_access:  write_only
        .address_space:  global
        .offset:         104
        .size:           8
        .value_kind:     global_buffer
      - .actual_access:  write_only
        .address_space:  global
        .offset:         112
        .size:           8
        .value_kind:     global_buffer
      - .actual_access:  write_only
        .address_space:  global
        .offset:         120
        .size:           8
        .value_kind:     global_buffer
      - .actual_access:  write_only
        .address_space:  global
        .offset:         128
        .size:           8
        .value_kind:     global_buffer
      - .address_space:  global
        .offset:         136
        .size:           8
        .value_kind:     global_buffer
      - .address_space:  global
        .offset:         144
        .size:           8
        .value_kind:     global_buffer
      - .actual_access:  write_only
        .address_space:  global
        .offset:         152
        .size:           8
        .value_kind:     global_buffer
    .group_segment_fixed_size: 46112
    .kernarg_segment_align: 8
    .kernarg_segment_size: 160
    .language:       OpenCL C
    .language_version:
      - 2
      - 0
    .max_flat_workgroup_size: 512
    .name:           _Z11proj_kernelPKfS0_S0_S0_S0_S0_S0_S0_S0_S0_S0_S0_S0_PfS1_PDF16_S1_S0_S0_S2_
    .private_segment_fixed_size: 0
    .sgpr_count:     33
    .sgpr_spill_count: 0
    .symbol:         _Z11proj_kernelPKfS0_S0_S0_S0_S0_S0_S0_S0_S0_S0_S0_S0_PfS1_PDF16_S1_S0_S0_S2_.kd
    .uniform_work_group_size: 1
    .uses_dynamic_stack: false
    .vgpr_count:     133
    .vgpr_spill_count: 0
    .wavefront_size: 64
  - .agpr_count:     0
    .args:
      - .actual_access:  read_only
        .address_space:  global
        .offset:         0
        .size:           8
        .value_kind:     global_buffer
      - .actual_access:  read_only
        .address_space:  global
        .offset:         8
        .size:           8
        .value_kind:     global_buffer
      - .actual_access:  read_only
        .address_space:  global
        .offset:         16
        .size:           8
        .value_kind:     global_buffer
      - .actual_access:  read_only
        .address_space:  global
        .offset:         24
        .size:           8
        .value_kind:     global_buffer
      - .actual_access:  read_only
        .address_space:  global
        .offset:         32
        .size:           8
        .value_kind:     global_buffer
      - .actual_access:  read_only
        .address_space:  global
        .offset:         40
        .size:           8
        .value_kind:     global_buffer
      - .actual_access:  read_only
        .address_space:  global
        .offset:         48
        .size:           8
        .value_kind:     global_buffer
      - .actual_access:  write_only
        .address_space:  global
        .offset:         56
        .size:           8
        .value_kind:     global_buffer
      - .actual_access:  write_only
        .address_space:  global
        .offset:         64
        .size:           8
        .value_kind:     global_buffer
    .group_segment_fixed_size: 0
    .kernarg_segment_align: 8
    .kernarg_segment_size: 72
    .language:       OpenCL C
    .language_version:
      - 2
      - 0
    .max_flat_workgroup_size: 768
    .name:           _Z11attn_kernelPKfS0_PKDF16_S0_S0_S0_S2_PDF16_S3_
    .private_segment_fixed_size: 0
    .sgpr_count:     70
    .sgpr_spill_count: 0
    .symbol:         _Z11attn_kernelPKfS0_PKDF16_S0_S0_S0_S2_PDF16_S3_.kd
    .uniform_work_group_size: 1
    .uses_dynamic_stack: false
    .vgpr_count:     168
    .vgpr_spill_count: 0
    .wavefront_size: 64
  - .agpr_count:     8
    .args:
      - .actual_access:  read_only
        .address_space:  global
        .offset:         0
        .size:           8
        .value_kind:     global_buffer
      - .actual_access:  read_only
        .address_space:  global
        .offset:         8
        .size:           8
        .value_kind:     global_buffer
      - .actual_access:  read_only
        .address_space:  global
        .offset:         16
        .size:           8
        .value_kind:     global_buffer
      - .actual_access:  write_only
        .address_space:  global
        .offset:         24
        .size:           8
        .value_kind:     global_buffer
    .group_segment_fixed_size: 27648
    .kernarg_segment_align: 8
    .kernarg_segment_size: 32
    .language:       OpenCL C
    .language_version:
      - 2
      - 0
    .max_flat_workgroup_size: 256
    .name:           _Z10out_kernelPKDF16_S0_PKfPf
    .private_segment_fixed_size: 0
    .sgpr_count:     18
    .sgpr_spill_count: 0
    .symbol:         _Z10out_kernelPKDF16_S0_PKfPf.kd
    .uniform_work_group_size: 1
    .uses_dynamic_stack: false
    .vgpr_count:     88
    .vgpr_spill_count: 0
    .wavefront_size: 64
